# DPP row_shr/row_bcast wave scans replace the 6-step ds_bpermute scans in sort1 and sort2 (instruction selection)
# speedup vs baseline: 1.0078x; 1.0078x over previous
.LBB0_25:
	s_or_b64 exec, exec, s[8:9]
	s_movk_i32 s3, 0x100
	v_cmp_gt_u32_e64 s[4:5], s3, v0
	s_and_saveexec_b64 s[6:7], s[4:5]
	v_mov_b32_e32 v2, 0
	ds_write_b32 v1, v2 offset:13536
	s_or_b64 exec, exec, s[6:7]
	s_waitcnt vmcnt(0)
	v_cmp_lt_i32_e64 s[8:9], -1, v16
	v_mov_b32_e32 v18, 0
	v_lshrrev_b32_e32 v24, 6, v16
	v_mov_b32_e32 v23, 0
	s_waitcnt lgkmcnt(0)
	s_barrier
	s_and_saveexec_b64 s[4:5], s[8:9]
	v_and_b32_e32 v2, 0x3fffffc, v24
	v_mov_b32_e32 v3, 1
	ds_add_rtn_u32 v23, v2, v3 offset:13536
	s_or_b64 exec, exec, s[4:5]
	v_cmp_lt_i32_e64 s[6:7], -1, v14
	v_lshrrev_b32_e32 v22, 6, v14
	s_and_saveexec_b64 s[4:5], s[6:7]
	v_and_b32_e32 v2, 0x3fffffc, v22
	v_mov_b32_e32 v3, 1
	ds_add_rtn_u32 v18, v2, v3 offset:13536
	s_or_b64 exec, exec, s[4:5]
	v_cmp_lt_i32_e64 s[4:5], -1, v12
	v_mov_b32_e32 v17, 0
	v_lshrrev_b32_e32 v21, 6, v12
	v_mov_b32_e32 v20, 0
	s_and_saveexec_b64 s[10:11], s[4:5]
	v_and_b32_e32 v2, 0x3fffffc, v21
	v_mov_b32_e32 v3, 1
	ds_add_rtn_u32 v20, v2, v3 offset:13536
	s_or_b64 exec, exec, s[10:11]
	v_cmp_lt_i32_e64 s[10:11], -1, v10
	v_lshrrev_b32_e32 v19, 6, v10
	s_and_saveexec_b64 s[12:13], s[10:11]
	v_and_b32_e32 v2, 0x3fffffc, v19
	v_mov_b32_e32 v3, 1
	ds_add_rtn_u32 v17, v2, v3 offset:13536
	s_or_b64 exec, exec, s[12:13]
	s_load_dwordx2 s[14:15], s[0:1], 0x58
	v_cmp_gt_u32_e64 s[12:13], 64, v0
	s_waitcnt lgkmcnt(0)
	s_barrier
	s_and_saveexec_b64 s[16:17], s[12:13]
	s_cbranch_execz .LBB0_44
	v_lshlrev_b32_e32 v25, 4, v0
	ds_read_b128 v[26:29], v25 offset:13536
	s_load_dwordx2 s[12:13], s[0:1], 0x50
	s_waitcnt lgkmcnt(0)
	v_add_u32_e32 v5, v27, v26
	v_add3_u32 v5, v5, v28, v29
	v_mov_b32_e32 v4, v5
	s_nop 1
	v_add_u32_dpp v4, v4, v4 row_shr:1 row_mask:0xf bank_mask:0xf
	s_nop 1
	v_add_u32_dpp v4, v4, v4 row_shr:2 row_mask:0xf bank_mask:0xf
	s_nop 1
	v_add_u32_dpp v4, v4, v4 row_shr:4 row_mask:0xf bank_mask:0xf
	s_nop 1
	v_add_u32_dpp v4, v4, v4 row_shr:8 row_mask:0xf bank_mask:0xf
	s_nop 1
	v_add_u32_dpp v4, v4, v4 row_bcast:15 row_mask:0xa bank_mask:0xf
	s_nop 1
	v_add_u32_dpp v4, v4, v4 row_bcast:31 row_mask:0xc bank_mask:0xf
	s_nop 1
	v_mov_b32_e32 v2, v4
	v_sub_u32_e32 v2, v2, v5
	v_add_u32_e32 v3, v2, v26
	v_add_u32_e32 v4, v3, v27
	v_add_u32_e32 v5, v4, v28
	v_cmp_gt_u32_e64 s[0:1], 50, v0
	ds_write_b128 v25, v[2:5] offset:12512
	s_and_saveexec_b64 s[18:19], s[0:1]
	s_cbranch_execz .LBB0_38
	v_lshl_add_u32 v26, v0, 10, s2
	v_ashrrev_i32_e32 v27, 31, v26
	v_lshl_add_u64 v[26:27], v[26:27], 2, s[12:13]
	global_store_dword v[26:27], v2, off

_Z12sort2_kernelPKfPDF16_PhS1_PKiPKjP15HIP_vector_typeIiLj4EEPiPt:
	s_cmpk_lt_i32 s2, 0xc4
	s_mov_b64 s[4:5], -1
	s_cbranch_scc0 .LBB1_103
	s_load_dwordx2 s[26:27], s[0:1], 0x40
	s_load_dwordx4 s[28:31], s[0:1], 0x30
	s_movk_i32 s3, 0x100
	v_and_b32_e32 v9, 63, v0
	v_lshrrev_b32_e32 v27, 6, v0
	v_cmp_gt_u32_e64 s[8:9], s3, v0
	v_lshlrev_b32_e32 v23, 2, v0
	s_and_saveexec_b64 s[4:5], s[8:9]
	s_cbranch_execz .LBB1_6
	s_load_dwordx2 s[6:7], s[0:1], 0x20
	s_lshl_b32 s10, s2, 8
	v_or_b32_e32 v2, s10, v0
	v_mov_b32_e32 v1, 0
	v_ashrrev_i32_e32 v3, 31, v2
	s_ashr_i32 s11, s10, 31
	s_waitcnt lgkmcnt(0)
	v_lshl_add_u64 v[4:5], v[2:3], 2, s[6:7]
	v_lshl_add_u64 v[2:3], s[10:11], 0, v[0:1]
	v_lshl_add_u64 v[6:7], v[2:3], 2, s[6:7]
	global_load_dword v2, v[4:5], off
	global_load_dword v3, v[6:7], off offset:1024
	v_cmp_gt_u32_e32 vcc, 64, v0
	ds_write_b32 v23, v1 offset:18432
	s_waitcnt vmcnt(0)
	ds_write2st64_b32 v23, v2, v3 offset0:64 offset1:68
	s_and_saveexec_b64 s[6:7], vcc
	ds_write_b32 v23, v1 offset:21504
	s_or_b64 exec, exec, s[6:7]
	v_mov_b32_e32 v1, v2
	s_nop 1
	v_add_u32_dpp v1, v1, v1 row_shr:1 row_mask:0xf bank_mask:0xf
	s_nop 1
	v_add_u32_dpp v1, v1, v1 row_shr:2 row_mask:0xf bank_mask:0xf
	s_nop 1
	v_add_u32_dpp v1, v1, v1 row_shr:4 row_mask:0xf bank_mask:0xf
	s_nop 1
	v_add_u32_dpp v1, v1, v1 row_shr:8 row_mask:0xf bank_mask:0xf
	s_nop 1
	v_add_u32_dpp v1, v1, v1 row_bcast:15 row_mask:0xa bank_mask:0xf
	s_nop 1
	v_add_u32_dpp v1, v1, v1 row_bcast:31 row_mask:0xc bank_mask:0xf
	s_nop 1
	v_mov_b32_e32 v2, 0
	v_cmp_eq_u32_e32 vcc, 63, v9
	s_and_b64 exec, exec, vcc
	s_cbranch_execz .LBB1_6
	s_waitcnt lgkmcnt(0)
	v_add_u32_e32 v1, v2, v1
	v_lshlrev_b32_e32 v2, 2, v27
	ds_write_b32 v2, v1 offset:21776

.LBB1_33:
	s_or_b64 exec, exec, s[24:25]
	s_lshl_b32 s3, s2, 8
	v_add_u32_e32 v8, s3, v0
	v_mov_b32_e32 v7, 0
	v_mov_b32_e32 v29, 0
	v_mov_b32_e32 v6, 0
	v_mov_b32_e32 v15, 0
	s_waitcnt lgkmcnt(0)
	s_barrier
	s_and_saveexec_b64 s[24:25], s[8:9]
	s_cbranch_execz .LBB1_39
	ds_read_b32 v7, v23 offset:18432
	s_waitcnt lgkmcnt(0)
	v_mov_b32_e32 v29, v7
	s_nop 1
	v_add_u32_dpp v29, v29, v29 row_shr:1 row_mask:0xf bank_mask:0xf
	s_nop 1
	v_add_u32_dpp v29, v29, v29 row_shr:2 row_mask:0xf bank_mask:0xf
	s_nop 1
	v_add_u32_dpp v29, v29, v29 row_shr:4 row_mask:0xf bank_mask:0xf
	s_nop 1
	v_add_u32_dpp v29, v29, v29 row_shr:8 row_mask:0xf bank_mask:0xf
	s_nop 1
	v_add_u32_dpp v29, v29, v29 row_bcast:15 row_mask:0xa bank_mask:0xf
	s_nop 1
	v_add_u32_dpp v29, v29, v29 row_bcast:31 row_mask:0xc bank_mask:0xf
	s_nop 1
	v_cmp_eq_u32_e64 s[22:23], 63, v9
	s_and_saveexec_b64 s[36:37], s[22:23]
	v_lshlrev_b32_e32 v6, 2, v27
	ds_write_b32 v6, v29 offset:21760
	s_or_b64 exec, exec, s[36:37]
	s_mov_b32 s22, 0xc350
	v_min_i32_e32 v6, 63, v7
	v_cmp_gt_i32_e64 s[22:23], s22, v8
	v_mov_b32_e32 v15, 0
	s_and_saveexec_b64 s[36:37], s[22:23]
	v_lshlrev_b32_e32 v15, 2, v6
	v_mov_b32_e32 v28, 1
	ds_add_rtn_u32 v15, v15, v28 offset:21504
	s_or_b64 exec, exec, s[36:37]

.LBB1_44:
	s_or_b64 exec, exec, s[38:39]
	v_sub_u32_e32 v27, v29, v7
	v_add_u32_e32 v28, v27, v28
	v_mov_b32_e32 v27, 0
	ds_write2st64_b32 v23, v27, v28 offset0:72 offset1:76
	s_and_saveexec_b64 s[24:25], s[22:23]
	s_cbranch_execz .LBB1_46
	ds_read_b32 v27, v23 offset:21504
	s_waitcnt lgkmcnt(0)
	v_mov_b32_e32 v9, v27
	s_nop 1
	v_add_u32_dpp v9, v9, v9 row_shr:1 row_mask:0xf bank_mask:0xf
	s_nop 1
	v_add_u32_dpp v9, v9, v9 row_shr:2 row_mask:0xf bank_mask:0xf
	s_nop 1
	v_add_u32_dpp v9, v9, v9 row_shr:4 row_mask:0xf bank_mask:0xf
	s_nop 1
	v_add_u32_dpp v9, v9, v9 row_shr:8 row_mask:0xf bank_mask:0xf
	s_nop 1
	v_add_u32_dpp v9, v9, v9 row_bcast:15 row_mask:0xa bank_mask:0xf
	s_nop 1
	v_add_u32_dpp v9, v9, v9 row_bcast:31 row_mask:0xc bank_mask:0xf
	s_nop 1
	v_sub_u32_e32 v9, v9, v27
	ds_write_b32 v23, v9 offset:21504
